# prologue queue: next unit index prefetched by an early global atomic (on top of mod ring)
# baseline (speedup 1.0000x reference)
.LBB0_5:
	s_or_b64 exec, exec, s[4:5]
	s_add_u32 s16, s14, 0x4060
	s_addc_u32 s17, s15, 0
	s_add_u32 s2, s14, 0x1d52ce00
	s_addc_u32 s3, s15, 0
	v_writelane_b32 v252, s2, 11
	s_load_dwordx16 s[36:51], s[0:1], 0x0
	v_mov_b32_e32 v11, 0
	v_writelane_b32 v252, s3, 12
	s_add_u32 s2, s14, 0x1c52ce00
	s_addc_u32 s3, s15, 0
	v_writelane_b32 v252, s2, 13
	v_mov_b32_e32 v1, 0x38d1b717
	v_mov_b32_e32 v78, 0x3c0881c4
	v_writelane_b32 v252, s3, 14
	s_add_u32 s2, s14, 0x1ac2ce00
	s_addc_u32 s3, s15, 0
	v_writelane_b32 v252, s2, 15
	v_mov_b32_e32 v79, 0xbab64f3b
	v_mov_b32_e32 v80, 0xc2f0cb68
	v_writelane_b32 v252, s3, 16
	s_add_u32 s2, s14, 0x79100
	v_writelane_b32 v252, s2, 17
	s_addc_u32 s2, s15, 0
	v_writelane_b32 v252, s2, 18
	s_add_u32 s2, s14, 0xa42ce00
	v_writelane_b32 v252, s2, 19
	s_addc_u32 s2, s15, 0
	v_writelane_b32 v252, s2, 20
	s_add_u32 s2, s14, 0x1d98ce00
	s_addc_u32 s3, s15, 0
	v_writelane_b32 v252, s2, 21
	v_mov_b32_e32 v82, 0x80000
	v_mov_b32_e32 v83, 0x150000
	v_writelane_b32 v252, s3, 22
	s_add_u32 s2, s14, 0x4100
	v_writelane_b32 v252, s2, 23
	s_addc_u32 s2, s15, 0
	v_writelane_b32 v252, s2, 24
	s_add_u32 s2, s14, 0x1542ce00
	v_writelane_b32 v252, s2, 25
	s_addc_u32 s2, s15, 0
	v_writelane_b32 v252, s2, 26
	s_add_u32 s2, s14, 0x1ef8ce00
	s_addc_u32 s3, s15, 0
	v_writelane_b32 v252, s2, 27
	v_mov_b32_e32 v84, 0x700
	v_mov_b32_e32 v85, 0x200
	v_writelane_b32 v252, s3, 28
	s_add_u32 s2, s14, 0xd9d00
	s_addc_u32 s3, s15, 0
	v_writelane_b32 v252, s2, 29
	v_mov_b32_e32 v86, 0x230000
	v_mov_b32_e32 v87, 6
	v_writelane_b32 v252, s3, 30
	s_add_u32 s2, s14, 0x27c8ce00
	v_writelane_b32 v252, s2, 31
	s_addc_u32 s2, s15, 0
	v_writelane_b32 v252, s2, 32
	s_add_u32 s2, s14, 0x27d8ce00
	v_writelane_b32 v252, s2, 33
	s_addc_u32 s2, s15, 0
	v_writelane_b32 v252, s2, 34
	s_add_u32 s2, s14, 0x1fa8ce00
	v_writelane_b32 v252, s2, 35
	s_addc_u32 s2, s15, 0
	v_writelane_b32 v252, s2, 36
	s_add_u32 s2, s14, 0x27a8ce00
	s_addc_u32 s3, s15, 0
	s_waitcnt lgkmcnt(0)
	s_add_u32 s18, s48, 0x60000
	s_addc_u32 s19, s49, 0
	s_load_dwordx16 s[36:51], s[0:1], 0x80
	v_writelane_b32 v252, s2, 37
	v_mov_b32_e32 v88, 0x6000000
	v_not_b32_e32 v89, 63
	v_writelane_b32 v252, s3, 38
	s_waitcnt lgkmcnt(0)
	s_add_u32 s2, s42, 0x110
	s_addc_u32 s3, s43, 0
	s_add_i32 s33, 0, 0x23fd0
	v_mov_b32_e32 v81, s33
	v_not_b32_e32 v90, 31
	v_mov_b32_e32 v91, 0xffc00000
	v_mov_b32_e32 v92, 0x7fc00000
	v_mov_b32_e32 v93, 0x7f800000
	s_movk_i32 s58, 0xdff
	s_movk_i32 s59, 0x13ff
	s_movk_i32 s60, 0x6000
	s_mov_b32 s61, 0xc000
	s_mov_b32 s62, 0x12000
	s_mov_b32 s63, 0x42fe0000
	s_movk_i32 s64, 0x2040
	s_mov_b32 s65, 0x40c0c00
	s_movk_i32 s66, 0x1000
	s_mov_b32 s67, 0x10000
	s_add_i32 s68, 0, 0x16100
	s_movk_i32 s69, 0x1600
	s_mov_b32 s70, 0x18000
	s_mov_b32 s71, 0x24000
	s_mov_b32 s72, 0x30000
	s_mov_b32 s73, 0x3c000
	s_mov_b32 s74, 0x437f0000
	s_brev_b32 s75, 18
	s_mov_b32 s76, 0xfe5163ab
	s_mov_b32 s77, 0x3c439041
	s_mov_b32 s78, 0xdb629599
	s_mov_b32 s79, 0xf534ddc0
	s_mov_b32 s80, 0xfc2757d1
	s_mov_b32 s81, 0x4e441529
	s_mov_b32 s82, 0xa2f9836e
	s_mov_b32 s83, 0x3fc90fda
	s_mov_b32 s84, 0x3f22f983
	s_mov_b32 s85, 0xbfc90fda
	s_brev_b32 s86, 1
	s_mov_b32 s87, 0x7f800000
	s_movk_i32 s88, 0x2100
	s_movk_i32 s89, 0x110
	s_add_i32 s90, 0, 0x2400
	s_movk_i32 s91, 0x1f8
	s_add_i32 s92, 0, 0x6800
	s_add_i32 s93, 0, 0xac00
	s_mov_b32 s94, 0xbb800000
	s_mov_b32 s95, 0x3fb8aa3b
	s_mov_b32 s96, 0xc2ce8ed0
	s_mov_b32 s97, 0x42b17218
	s_mov_b32 s57, 0x467ffc00
	s_mov_b32 s22, 0xb8800000
	s_mov_b32 s21, 0
	v_cmp_eq_u32_e32 vcc, 0, v0
	s_and_saveexec_b64 s[4:5], vcc
	v_mov_b32_e32 v2, 1
	s_nop 0
	global_atomic_add v200, v11, v2, s[16:17] sc0
	s_mov_b64 exec, s[4:5]
	s_branch .LBB0_8

.LBB0_8:
	s_waitcnt lgkmcnt(0)
	s_barrier
	v_mov_b32_e32 v2, v0
	s_nop 0
	v_cmp_eq_u32_e32 vcc, 0, v2
	s_and_saveexec_b64 s[4:5], vcc
	s_cbranch_execz .LBB0_12
	s_waitcnt vmcnt(0)
	v_mov_b32_e32 v3, s33
	v_readfirstlane_b32 s6, v200
	ds_write_b32 v3, v200
	s_cmpk_gt_u32 s6, 0x1619
	s_cbranch_scc1 .Lqpf_skip
	v_mov_b32_e32 v2, 1
	s_nop 0
	global_atomic_add v200, v11, v2, s[16:17] sc0
.Lqpf_skip:
.LBB0_12:
	s_or_b64 exec, exec, s[4:5]
	s_waitcnt lgkmcnt(0)
	s_barrier
	ds_read_b32 v2, v81
	s_movk_i32 s4, 0x1619
	s_waitcnt lgkmcnt(0)
	v_cmp_lt_i32_e32 vcc, s4, v2
	v_readfirstlane_b32 s56, v2
	s_mov_b64 s[4:5], -1
	s_cbranch_vccnz .LBB0_7
	s_mul_hi_i32 s4, s56, 0x38e38e39
	s_lshr_b32 s5, s4, 31
	s_ashr_i32 s23, s4, 1
	s_add_i32 s23, s23, s5
	s_mul_i32 s4, s23, 9
	s_sub_i32 s4, s56, s4
	s_cmp_lg_u32 s4, 0
	s_cselect_b64 s[4:5], -1, 0
	s_cmpk_gt_i32 s56, 0x1223
	s_cselect_b64 s[6:7], -1, 0
	s_or_b64 s[6:7], s[4:5], s[6:7]
	s_mov_b64 s[4:5], -1
	s_and_b64 vcc, exec, s[6:7]
	s_cbranch_vccz .LBB0_292
	s_add_i32 s4, s56, 8
	s_mul_hi_i32 s4, s4, 0x38e38e39
	s_lshr_b32 s5, s4, 31
	s_ashr_i32 s4, s4, 1
	s_add_i32 s4, s4, s5
	s_min_i32 s4, s4, 0x204
	s_sub_i32 s36, s56, s4
	s_cmpk_gt_i32 s36, 0x5f
	s_mov_b64 s[4:5], -1
	s_cbranch_scc0 .LBB0_254
	s_cmpk_gt_u32 s36, 0x4df
	s_cbranch_scc0 .LBB0_240
	s_cmpk_gt_u32 s36, 0x113f
	s_cbranch_scc0 .LBB0_224
	s_cmpk_gt_u32 s36, 0x12cf
	s_cbranch_scc0 .LBB0_185
	v_mov_b32_e32 v3, v0
	s_lshl_b32 s4, s36, 3
	s_add_i32 s4, s4, 0xffff6980
	v_ashrrev_i32_e32 v4, 6, v3
	v_add_u32_e32 v2, s4, v4
	s_movk_i32 s4, 0xa30
	v_cmp_gt_i32_e32 vcc, s4, v2
	s_and_saveexec_b64 s[8:9], vcc
	s_cbranch_execz .LBB0_184
	s_movk_i32 s4, 0x4400
	v_and_b32_e32 v95, 63, v3
	v_mul_lo_u32 v4, v4, s4
	s_movk_i32 s4, 0x7ff
	v_lshlrev_b32_e32 v3, 2, v95
	v_add_u32_e32 v94, 0, v4
	v_cmp_lt_i32_e32 vcc, s4, v2
	v_lshrrev_b32_e32 v96, 4, v95
	v_and_b32_e32 v97, 60, v3
	s_and_saveexec_b64 s[4:5], vcc
	s_xor_b64 s[10:11], exec, s[4:5]
	s_cbranch_execz .LBB0_181
	v_add_u32_e32 v3, 0xfffff800, v2
	s_movk_i32 s4, 0x118
	v_add_u32_e32 v2, 0xf6e8, v2
	v_cmp_gt_u32_e32 vcc, s4, v3
	s_mov_b32 s4, 0xcccd
	s_load_dwordx16 s[40:55], s[0:1], 0x80
	v_cndmask_b32_e32 v6, v2, v3, vcc
	v_mul_u32_u24_sdwa v2, v6, s4 dst_sel:DWORD dst_unused:UNUSED_PAD src0_sel:WORD_0 src1_sel:DWORD
	v_lshrrev_b32_e32 v2, 19, v2
	s_movk_i32 s4, 0x117
	v_mul_lo_u16_e32 v4, 10, v2
	v_cmp_lt_u32_e32 vcc, s4, v3
	v_lshlrev_b32_e32 v98, 6, v2
	v_sub_u16_e32 v100, v6, v4
	v_cndmask_b32_e32 v10, 0, v82, vcc
	v_or_b32_e32 v3, v98, v97
	s_waitcnt lgkmcnt(0)
	v_lshl_add_u64 v[4:5], s[42:43], 0, v[10:11]
	v_lshlrev_b16_e32 v99, 6, v100
	s_movk_i32 s4, 0x77
	v_lshlrev_b32_e32 v10, 2, v3
	v_or_b32_e32 v2, v96, v99
	v_cmp_lt_u16_e64 s[4:5], s4, v6
	v_lshl_add_u64 v[4:5], v[4:5], 0, v[10:11]
	s_mov_b64 s[24:25], 0
	s_and_saveexec_b64 s[6:7], s[4:5]
	s_xor_b64 s[26:27], exec, s[6:7]
	s_cbranch_execz .LBB0_24
	v_cmp_lt_u16_e64 s[6:7], 7, v100
	s_and_saveexec_b64 s[28:29], s[6:7]
	s_xor_b64 s[6:7], exec, s[28:29]
	v_add_u32_e32 v18, 0xfffffe00, v2
	v_mov_b32_e32 v19, v11
	v_lshlrev_b64 v[6:7], 12, v[18:19]
	s_movk_i32 s28, 0xf400
	v_lshl_add_u64 v[6:7], v[4:5], 0, v[6:7]
	s_mov_b32 s29, -1
	s_mov_b64 s[24:25], exec
	v_lshl_add_u64 v[20:21], v[6:7], 0, s[28:29]
	s_or_b64 exec, exec, s[6:7]
	s_and_b64 s[24:25], s[24:25], exec
